# softmax max/sum cross-row reductions via v_permlane16/32_swap instead of ds_bpermute
# baseline (speedup 1.0000x reference)
_Z7na_mainPKDF16_PKhS0_PKfS4_S4_S4_Pf:
	s_lshl_b32 s3, s2, 5
	s_and_b32 s3, s3, 0xe0
	s_ashr_i32 s2, s2, 3
	s_add_i32 s3, s3, s2
	s_ashr_i32 s2, s3, 6
	s_lshl_b32 s3, s3, 5
	s_and_b32 s14, s3, 0x7e0
	v_mov_b32_e32 v1, 0x7c0
	s_load_dwordx8 s[4:11], s[0:1], 0x0
	s_load_dwordx2 s[18:19], s[0:1], 0x20
	v_med3_u32 v1, s14, 32, v1
	v_subrev_u32_e32 v97, 32, v1
	s_ashr_i32 s3, s2, 31
	v_lshlrev_b32_e32 v58, 1, v97
	s_lshl_b64 s[12:13], s[2:3], 12
	v_mov_b32_e32 v59, 0
	v_sub_u32_e32 v60, s14, v97
	v_lshl_add_u64 v[10:11], s[12:13], 0, v[58:59]
	v_lshlrev_b64 v[2:3], 9, v[10:11]
	v_lshl_or_b32 v22, v60, 6, v0
	s_waitcnt lgkmcnt(0)
	v_and_b32_e32 v208, 31, v0
	v_lshlrev_b32_e32 v208, 5, v208
	global_load_dwordx4 v[192:195], v208, s[18:19]
	global_load_dwordx4 v[196:199], v208, s[18:19] offset:16
	v_lshl_add_u64 v[20:21], s[4:5], 0, v[2:3]
	v_ashrrev_i32_e32 v23, 31, v22
	v_lshl_add_u64 v[2:3], v[22:23], 4, v[20:21]
	global_load_dwordx4 v[12:15], v[2:3], off
	v_or_b32_e32 v28, 0x200, v22
	v_ashrrev_i32_e32 v29, 31, v28
	v_lshl_add_u64 v[2:3], v[28:29], 4, v[20:21]
	global_load_dwordx4 v[16:19], v[2:3], off
	v_or_b32_e32 v184, 0x400, v22
	v_ashrrev_i32_e32 v185, 31, v184
	v_lshl_add_u64 v[184:185], v[184:185], 4, v[20:21]
	v_or_b32_e32 v188, 0x600, v22
	v_ashrrev_i32_e32 v189, 31, v188
	v_lshl_add_u64 v[188:189], v[188:189], 4, v[20:21]
	global_load_dwordx4 v[184:187], v[184:185], off
	global_load_dwordx4 v[188:191], v[188:189], off
	v_lshrrev_b32_e32 v99, 6, v0
	v_and_b32_e32 v98, 63, v0
	v_lshlrev_b32_e32 v118, 13, v99
	v_lshl_or_b32 v58, v98, 5, v118
	s_movk_i32 s15, 0x1000
	v_lshl_add_u64 v[24:25], s[6:7], 0, v[58:59]
	v_or_b32_e32 v32, 0x400, v22
	v_or_b32_e32 v62, 0x600, v22
	v_add_co_u32_e32 v64, vcc, s15, v24
	s_mov_b64 s[12:13], 0x1000
	s_mov_b64 s[16:17], 0x1800
	v_lshlrev_b32_e32 v72, 1, v60
	v_lshrrev_b32_e32 v23, 5, v22
	v_and_b32_e32 v34, 32, v22
	v_ashrrev_i32_e32 v33, 31, v32
	v_ashrrev_i32_e32 v63, 31, v62
	v_addc_co_u32_e32 v65, vcc, 0, v25, vcc
	global_load_dwordx4 v[6:9], v58, s[6:7] offset:16
	global_load_dwordx4 v[2:5], v58, s[6:7]
	global_load_dwordx4 v[54:57], v58, s[6:7] offset:2064
	global_load_dwordx4 v[50:53], v58, s[6:7] offset:2048
	v_lshrrev_b32_e32 v58, 6, v22
	v_bfe_u32 v73, v22, 8, 2
	v_lshl_add_u64 v[26:27], v[24:25], 0, s[12:13]
	v_lshl_add_u64 v[24:25], v[24:25], 0, s[16:17]
	v_cmp_ne_u32_e32 vcc, 0, v34
	v_sub_u32_e32 v75, v23, v72
	global_load_dwordx4 v[42:45], v[64:65], off
	global_load_dwordx4 v[46:49], v[26:27], off offset:16
	global_load_dwordx4 v[34:37], v[64:65], off offset:2048
	global_load_dwordx4 v[38:41], v[24:25], off offset:16
	v_mov_b32_e32 v61, 0x60
	v_cndmask_b32_e32 v74, 0, v61, vcc
	v_add_u32_e32 v33, v74, v58
	v_lshlrev_b32_e32 v64, 2, v33
	v_bfe_u32 v96, v0, 4, 1
	v_and_b32_e32 v100, 15, v0
	v_mov_b32_e32 v30, v59
	v_mov_b32_e32 v31, v59
	v_and_b32_e32 v64, 12, v64
	v_mul_u32_u24_e32 v29, 0xc000, v96
	v_bitop3_b32 v64, v64, v100, v73 bitop3:0x36
	v_lshl_or_b32 v64, v64, 4, v29
	v_lshlrev_b32_e32 v63, 1, v75
	v_lshl_add_u32 v33, v33, 8, v64
	v_bfe_u32 v71, v0, 1, 4
	v_and_b32_e32 v70, 32, v0
	v_lshlrev_b32_e32 v1, 3, v0
	v_lshrrev_b32_e32 v58, 1, v75
	v_and_b32_e32 v1, 8, v1
	v_add_lshl_u32 v58, v58, v70, 8
	v_lshlrev_b32_e32 v121, 3, v99
	v_bfe_u32 v101, v0, 4, 2
	v_lshlrev_b32_e32 v102, 2, v101
	v_and_b32_e32 v116, 31, v0
	v_bfe_u32 v119, v0, 5, 1
	v_lshlrev_b32_e32 v124, 1, v119
	v_lshlrev_b32_e32 v117, 8, v116
	v_lshrrev_b32_e32 v95, 4, v0
	s_movk_i32 s16, 0x60
	s_mov_b32 s17, 0xc000
	s_waitcnt vmcnt(11)
	v_fma_mix_f32 v200, v192, v12, 0 op_sel_hi:[0,1,0]
	v_fma_mix_f32 v201, v193, v12, 0 op_sel:[0,1,0] op_sel_hi:[0,1,0]
	v_fma_mix_f32 v200, v194, v13, v200 op_sel_hi:[0,1,0]
	v_fma_mix_f32 v201, v195, v13, v201 op_sel:[0,1,0] op_sel_hi:[0,1,0]
	v_fma_mix_f32 v200, v196, v14, v200 op_sel_hi:[0,1,0]
	v_fma_mix_f32 v201, v197, v14, v201 op_sel:[0,1,0] op_sel_hi:[0,1,0]
	v_fma_mix_f32 v200, v198, v15, v200 op_sel_hi:[0,1,0]
	v_fma_mix_f32 v201, v199, v15, v201 op_sel:[0,1,0] op_sel_hi:[0,1,0]
	v_cvt_f32_f16_e32 v65, v12
	v_cvt_f32_f16_sdwa v66, v12 dst_sel:DWORD dst_unused:UNUSED_PAD src0_sel:WORD_1
	v_cvt_f32_f16_e32 v69, v14
	v_cvt_f32_f16_sdwa v74, v14 dst_sel:DWORD dst_unused:UNUSED_PAD src0_sel:WORD_1
	v_cvt_f32_f16_e32 v67, v13
	v_cvt_f32_f16_sdwa v68, v13 dst_sel:DWORD dst_unused:UNUSED_PAD src0_sel:WORD_1
	v_cvt_f32_f16_e32 v76, v15
	v_cvt_f32_f16_sdwa v77, v15 dst_sel:DWORD dst_unused:UNUSED_PAD src0_sel:WORD_1
	v_cvt_pk_fp8_f32 v30, v65, v66
	v_cvt_pk_fp8_f32 v31, v69, v74
	ds_write_b128 v33, v[12:15]
	v_and_b32_e32 v12, 12, v63
	v_bfe_u32 v13, v75, 3, 2
	v_cvt_pk_fp8_f32 v30, v67, v68 op_sel:[0,0,1]
	v_cvt_pk_fp8_f32 v31, v76, v77 op_sel:[0,0,1]
	v_bitop3_b32 v12, v12, v71, v13 bitop3:0x36
	v_lshlrev_b32_e32 v12, 4, v12
	v_or3_b32 v12, v58, v12, v1
	v_add_u32_e32 v12, 0x23800, v12
	ds_write_b64 v12, v[30:31]
	v_and_b32_e32 v12, 32, v28
	v_cmp_ne_u32_e32 vcc, 0, v12
	v_lshrrev_b32_e32 v13, 6, v28
	v_bfe_u32 v15, v28, 8, 2
	v_cndmask_b32_e32 v12, 0, v61, vcc
	v_add_u32_e32 v12, v12, v13
	v_lshlrev_b32_e32 v13, 2, v12
	v_and_b32_e32 v13, 12, v13
	v_bitop3_b32 v13, v13, v100, v15 bitop3:0x36
	v_lshl_or_b32 v13, v13, 4, v29
	v_lshl_add_u32 v12, v12, 8, v13
	s_waitcnt vmcnt(10)
	v_fma_mix_f32 v202, v192, v16, 0 op_sel_hi:[0,1,0]
	v_fma_mix_f32 v203, v193, v16, 0 op_sel:[0,1,0] op_sel_hi:[0,1,0]
	v_fma_mix_f32 v202, v194, v17, v202 op_sel_hi:[0,1,0]
	v_fma_mix_f32 v203, v195, v17, v203 op_sel:[0,1,0] op_sel_hi:[0,1,0]
	v_fma_mix_f32 v202, v196, v18, v202 op_sel_hi:[0,1,0]
	v_fma_mix_f32 v203, v197, v18, v203 op_sel:[0,1,0] op_sel_hi:[0,1,0]
	v_fma_mix_f32 v202, v198, v19, v202 op_sel_hi:[0,1,0]
	v_fma_mix_f32 v203, v199, v19, v203 op_sel:[0,1,0] op_sel_hi:[0,1,0]
	v_cvt_f32_f16_e32 v13, v16
	v_cvt_f32_f16_sdwa v15, v16 dst_sel:DWORD dst_unused:UNUSED_PAD src0_sel:WORD_1
	ds_write_b128 v12, v[16:19]
	v_mov_b32_e32 v12, v59
	v_cvt_f32_f16_e32 v16, v17
	v_cvt_pk_fp8_f32 v12, v13, v15
	v_cvt_f32_f16_e32 v15, v18
	v_cvt_f32_f16_sdwa v18, v18 dst_sel:DWORD dst_unused:UNUSED_PAD src0_sel:WORD_1
	v_cvt_f32_f16_sdwa v17, v17 dst_sel:DWORD dst_unused:UNUSED_PAD src0_sel:WORD_1
	v_mov_b32_e32 v13, v59
	v_lshrrev_b32_e32 v14, 5, v28
	v_cvt_f32_f16_e32 v28, v19
	v_cvt_f32_f16_sdwa v19, v19 dst_sel:DWORD dst_unused:UNUSED_PAD src0_sel:WORD_1
	v_cvt_pk_fp8_f32 v13, v15, v18
	v_sub_u32_e32 v14, v14, v72
	v_cvt_pk_fp8_f32 v12, v16, v17 op_sel:[0,0,1]
	v_lshlrev_b32_e32 v16, 1, v14
	v_lshrrev_b32_e32 v15, 1, v14
	v_and_b32_e32 v16, 12, v16
	v_bfe_u32 v14, v14, 3, 2
	v_cvt_pk_fp8_f32 v13, v28, v19 op_sel:[0,0,1]
	v_bitop3_b32 v14, v16, v71, v14 bitop3:0x36
	v_add_lshl_u32 v15, v15, v70, 8
	v_lshlrev_b32_e32 v14, 4, v14
	v_or3_b32 v14, v15, v14, v1
	v_add_u32_e32 v14, 0x23800, v14
	ds_write_b64 v14, v[12:13]
	v_and_b32_e32 v12, 32, v32
	v_cmp_ne_u32_e32 vcc, 0, v12
	v_lshrrev_b32_e32 v13, 6, v32
	s_waitcnt vmcnt(9)
	v_fma_mix_f32 v204, v192, v184, 0 op_sel_hi:[0,1,0]
	v_fma_mix_f32 v205, v193, v184, 0 op_sel:[0,1,0] op_sel_hi:[0,1,0]
	v_fma_mix_f32 v204, v194, v185, v204 op_sel_hi:[0,1,0]
	v_fma_mix_f32 v205, v195, v185, v205 op_sel:[0,1,0] op_sel_hi:[0,1,0]
	v_fma_mix_f32 v204, v196, v186, v204 op_sel_hi:[0,1,0]
	v_fma_mix_f32 v205, v197, v186, v205 op_sel:[0,1,0] op_sel_hi:[0,1,0]
	v_fma_mix_f32 v204, v198, v187, v204 op_sel_hi:[0,1,0]
	v_fma_mix_f32 v205, v199, v187, v205 op_sel:[0,1,0] op_sel_hi:[0,1,0]
	v_cvt_f32_f16_sdwa v15, v184 dst_sel:DWORD dst_unused:UNUSED_PAD src0_sel:WORD_1
	v_cndmask_b32_e32 v12, 0, v61, vcc
	v_add_u32_e32 v12, v12, v13
	v_lshlrev_b32_e32 v13, 2, v12
	v_and_b32_e32 v13, 12, v13
	v_bitop3_b32 v13, v13, v100, v73 bitop3:0x36
	v_lshl_or_b32 v13, v13, 4, v29
	v_lshl_add_u32 v12, v12, 8, v13
	v_cvt_f32_f16_e32 v13, v184
	ds_write_b128 v12, v[184:187]
	v_mov_b32_e32 v12, v59
	v_cvt_f32_f16_sdwa v18, v186 dst_sel:DWORD dst_unused:UNUSED_PAD src0_sel:WORD_1
	v_cvt_pk_fp8_f32 v12, v13, v15
	v_cvt_f32_f16_e32 v15, v186
	v_cvt_f32_f16_e32 v16, v185
	v_cvt_f32_f16_sdwa v17, v185 dst_sel:DWORD dst_unused:UNUSED_PAD src0_sel:WORD_1
	v_mov_b32_e32 v13, v59
	v_lshrrev_b32_e32 v14, 5, v32
	v_cvt_f32_f16_e32 v19, v187
	v_cvt_f32_f16_sdwa v20, v187 dst_sel:DWORD dst_unused:UNUSED_PAD src0_sel:WORD_1
	v_cvt_pk_fp8_f32 v13, v15, v18
	v_sub_u32_e32 v14, v14, v72
	v_cvt_pk_fp8_f32 v12, v16, v17 op_sel:[0,0,1]
	v_lshlrev_b32_e32 v16, 1, v14
	v_lshrrev_b32_e32 v15, 1, v14
	v_and_b32_e32 v16, 12, v16
	v_bfe_u32 v14, v14, 3, 2
	v_cvt_pk_fp8_f32 v13, v19, v20 op_sel:[0,0,1]
	v_bitop3_b32 v14, v16, v71, v14 bitop3:0x36
	v_add_lshl_u32 v15, v15, v70, 8
	v_lshlrev_b32_e32 v14, 4, v14
	v_or3_b32 v14, v15, v14, v1
	v_add_u32_e32 v14, 0x23800, v14
	ds_write_b64 v14, v[12:13]
	v_and_b32_e32 v12, 32, v62
	v_cmp_ne_u32_e32 vcc, 0, v12
	v_lshrrev_b32_e32 v13, 6, v62
	v_bfe_u32 v15, v62, 8, 2
	v_cndmask_b32_e32 v12, 0, v61, vcc
	v_add_u32_e32 v12, v12, v13
	v_lshlrev_b32_e32 v13, 2, v12
	v_and_b32_e32 v13, 12, v13
	v_bitop3_b32 v13, v13, v100, v15 bitop3:0x36
	v_lshl_or_b32 v13, v13, 4, v29
	v_lshl_add_u32 v12, v12, 8, v13
	s_waitcnt vmcnt(8)
	v_fma_mix_f32 v206, v192, v188, 0 op_sel_hi:[0,1,0]
	v_fma_mix_f32 v207, v193, v188, 0 op_sel:[0,1,0] op_sel_hi:[0,1,0]
	v_fma_mix_f32 v206, v194, v189, v206 op_sel_hi:[0,1,0]
	v_fma_mix_f32 v207, v195, v189, v207 op_sel:[0,1,0] op_sel_hi:[0,1,0]
	v_fma_mix_f32 v206, v196, v190, v206 op_sel_hi:[0,1,0]
	v_fma_mix_f32 v207, v197, v190, v207 op_sel:[0,1,0] op_sel_hi:[0,1,0]
	v_fma_mix_f32 v206, v198, v191, v206 op_sel_hi:[0,1,0]
	v_fma_mix_f32 v207, v199, v191, v207 op_sel:[0,1,0] op_sel_hi:[0,1,0]
	v_cvt_f32_f16_e32 v13, v188
	v_cvt_f32_f16_sdwa v15, v188 dst_sel:DWORD dst_unused:UNUSED_PAD src0_sel:WORD_1
	ds_write_b128 v12, v[188:191]
	v_mov_b32_e32 v12, v59
	v_cvt_f32_f16_sdwa v18, v190 dst_sel:DWORD dst_unused:UNUSED_PAD src0_sel:WORD_1
	v_cvt_pk_fp8_f32 v12, v13, v15
	v_cvt_f32_f16_e32 v15, v190
	v_cvt_f32_f16_e32 v16, v189
	v_cvt_f32_f16_sdwa v17, v189 dst_sel:DWORD dst_unused:UNUSED_PAD src0_sel:WORD_1
	v_mov_b32_e32 v13, v59
	v_lshrrev_b32_e32 v14, 5, v62
	v_cvt_f32_f16_e32 v19, v191
	v_cvt_f32_f16_sdwa v20, v191 dst_sel:DWORD dst_unused:UNUSED_PAD src0_sel:WORD_1
	v_cvt_pk_fp8_f32 v13, v15, v18
	v_sub_u32_e32 v14, v14, v72
	v_cvt_pk_fp8_f32 v12, v16, v17 op_sel:[0,0,1]
	v_lshlrev_b32_e32 v16, 1, v14
	v_lshrrev_b32_e32 v15, 1, v14
	v_and_b32_e32 v16, 12, v16
	v_bfe_u32 v14, v14, 3, 2
	v_cvt_pk_fp8_f32 v13, v19, v20 op_sel:[0,0,1]
	v_bitop3_b32 v14, v16, v71, v14 bitop3:0x36
	v_add_lshl_u32 v15, v15, v70, 8
	v_lshlrev_b32_e32 v14, 4, v14
	v_or3_b32 v14, v15, v14, v1
	v_add_u32_e32 v14, 0x23800, v14
	v_add_f32_e32 v200, v200, v201
	v_add_f32_e32 v202, v202, v203
	v_add_f32_e32 v204, v204, v205
	v_add_f32_e32 v206, v206, v207
	v_lshlrev_b32_e32 v208, 7, v119
	v_lshl_add_u32 v208, v99, 2, v208
	v_add_u32_e32 v208, 0x27800, v208
	v_add_f32_dpp v200, v200, v200 quad_perm:[1,0,3,2] row_mask:0xf bank_mask:0xf
	v_add_f32_dpp v202, v202, v202 quad_perm:[1,0,3,2] row_mask:0xf bank_mask:0xf
	v_add_f32_dpp v204, v204, v204 quad_perm:[1,0,3,2] row_mask:0xf bank_mask:0xf
	v_add_f32_dpp v206, v206, v206 quad_perm:[1,0,3,2] row_mask:0xf bank_mask:0xf
	v_add_f32_dpp v200, v200, v200 quad_perm:[2,3,0,1] row_mask:0xf bank_mask:0xf
	v_add_f32_dpp v202, v202, v202 quad_perm:[2,3,0,1] row_mask:0xf bank_mask:0xf
	v_add_f32_dpp v204, v204, v204 quad_perm:[2,3,0,1] row_mask:0xf bank_mask:0xf
	v_add_f32_dpp v206, v206, v206 quad_perm:[2,3,0,1] row_mask:0xf bank_mask:0xf
	v_add_f32_dpp v200, v200, v200 row_half_mirror row_mask:0xf bank_mask:0xf
	v_add_f32_dpp v202, v202, v202 row_half_mirror row_mask:0xf bank_mask:0xf
	v_add_f32_dpp v204, v204, v204 row_half_mirror row_mask:0xf bank_mask:0xf
	v_add_f32_dpp v206, v206, v206 row_half_mirror row_mask:0xf bank_mask:0xf
	v_add_f32_dpp v200, v200, v200 row_mirror row_mask:0xf bank_mask:0xf
	v_add_f32_dpp v202, v202, v202 row_mirror row_mask:0xf bank_mask:0xf
	v_add_f32_dpp v204, v204, v204 row_mirror row_mask:0xf bank_mask:0xf
	v_add_f32_dpp v206, v206, v206 row_mirror row_mask:0xf bank_mask:0xf
	v_add_f32_dpp v200, v200, v200 row_bcast:15 row_mask:0xa bank_mask:0xf
	v_add_f32_dpp v202, v202, v202 row_bcast:15 row_mask:0xa bank_mask:0xf
	v_add_f32_dpp v204, v204, v204 row_bcast:15 row_mask:0xa bank_mask:0xf
	v_add_f32_dpp v206, v206, v206 row_bcast:15 row_mask:0xa bank_mask:0xf
	s_mov_b32 exec_lo, 0xffff0000
	s_mov_b32 exec_hi, 0xffff0000
	ds_write_b32 v208, v200
	ds_write_b32 v208, v202 offset:32
	ds_write_b32 v208, v204 offset:64
	ds_write_b32 v208, v206 offset:96
	s_mov_b64 exec, -1
	v_cmp_lt_i32_e32 vcc, v121, v60
	ds_write_b64 v14, v[12:13]
	v_mov_b32_e32 v15, v59
	v_cndmask_b32_e64 v12, 32, 0, vcc
	v_add_u32_e32 v16, v12, v121
	v_or_b32_e32 v12, v16, v101
	v_lshlrev_b32_e32 v58, 1, v12
	v_lshrrev_b32_e32 v12, 5, v0
	v_and_b32_e32 v12, 2, v12
	v_bitop3_b32 v14, v102, v100, v12 bitop3:0x36
	v_lshl_add_u64 v[12:13], v[10:11], 0, v[58:59]
	v_lshlrev_b64 v[12:13], 9, v[12:13]
	v_lshlrev_b32_e32 v16, 8, v16
	v_lshl_add_u64 v[12:13], s[4:5], 0, v[12:13]
	v_lshlrev_b32_e32 v14, 4, v14
	v_readfirstlane_b32 s6, v16
	v_add_u32_e32 v17, 0xc000, v16
	v_lshl_add_u64 v[12:13], v[12:13], 0, v[14:15]
	s_mov_b32 m0, s6
	s_mov_b64 s[6:7], 0x100
	v_readfirstlane_b32 s12, v17
	global_load_lds_dwordx4 v[12:13], off
	v_lshl_add_u64 v[12:13], v[12:13], 0, s[6:7]
	s_mov_b32 m0, s12
	v_or_b32_e32 v58, 1, v58
	global_load_lds_dwordx4 v[12:13], off
	v_lshl_add_u64 v[12:13], v[10:11], 0, v[58:59]
	v_lshlrev_b64 v[12:13], 9, v[12:13]
	v_lshl_add_u64 v[12:13], s[4:5], 0, v[12:13]
	v_lshl_add_u64 v[12:13], v[12:13], 0, v[14:15]
	v_add_u32_e32 v14, 0x6000, v16
	v_bfe_u32 v61, v0, 2, 2
	v_readfirstlane_b32 s12, v14
	v_add_u32_e32 v14, 0x12000, v16
	s_mov_b32 m0, s12
	v_readfirstlane_b32 s12, v14
	global_load_lds_dwordx4 v[12:13], off
	v_lshl_add_u64 v[12:13], v[12:13], 0, s[6:7]
	s_mov_b32 m0, s12
	v_add_u32_e32 v18, 0x23800, v117
	global_load_lds_dwordx4 v[12:13], off
	v_or_b32_e32 v12, 4, v121
	v_cmp_lt_i32_e32 vcc, v12, v60
	s_nop 1
	v_cndmask_b32_e64 v13, 32, 0, vcc
	v_add_u32_e32 v16, v13, v12
	v_or_b32_e32 v13, v16, v101
	v_lshlrev_b32_e32 v58, 1, v13
	v_bfe_u32 v12, v12, 2, 2
	v_bitop3_b32 v14, v102, v100, v12 bitop3:0x36
	v_lshl_add_u64 v[12:13], v[10:11], 0, v[58:59]
	v_lshlrev_b64 v[12:13], 9, v[12:13]
	v_lshlrev_b32_e32 v16, 8, v16
	v_lshl_add_u64 v[12:13], s[4:5], 0, v[12:13]
	v_lshlrev_b32_e32 v14, 4, v14
	v_readfirstlane_b32 s12, v16
	v_add_u32_e32 v17, 0xc000, v16
	v_lshl_add_u64 v[12:13], v[12:13], 0, v[14:15]
	s_mov_b32 m0, s12
	v_readfirstlane_b32 s12, v17
	v_or_b32_e32 v58, 1, v58
	global_load_lds_dwordx4 v[12:13], off
	v_lshl_add_u64 v[12:13], v[12:13], 0, s[6:7]
	s_mov_b32 m0, s12
	v_lshl_add_u64 v[10:11], v[10:11], 0, v[58:59]
	global_load_lds_dwordx4 v[12:13], off
	v_lshlrev_b64 v[10:11], 9, v[10:11]
	v_add_u32_e32 v12, 0x6000, v16
	v_lshl_add_u64 v[10:11], s[4:5], 0, v[10:11]
	v_readfirstlane_b32 s4, v12
	v_add_u32_e32 v12, 0x12000, v16
	v_lshl_add_u64 v[10:11], v[10:11], 0, v[14:15]
	s_mov_b32 m0, s4
	v_readfirstlane_b32 s4, v12
	global_load_lds_dwordx4 v[10:11], off
	v_lshl_add_u64 v[10:11], v[10:11], 0, s[6:7]
	s_mov_b32 m0, s4
	s_nop 0
	global_load_lds_dwordx4 v[10:11], off
	s_waitcnt lgkmcnt(0)
	s_barrier
	v_lshlrev_b32_e32 v10, 2, v0
	v_and_b32_e32 v94, 12, v10
	v_or_b32_e32 v120, v94, v61
	v_bitop3_b32 v10, v124, v94, v61 bitop3:0x1e
	v_lshl_or_b32 v14, v10, 4, v18
	v_bitop3_b32 v10, v124, v120, 1 bitop3:0x36
	v_lshl_or_b32 v19, v10, 4, v18
	s_load_dwordx4 s[4:7], s[0:1], 0x20
	s_load_dwordx2 s[12:13], s[0:1], 0x38
	ds_read_b128 v[10:13], v14
	ds_read_b128 v[62:65], v14 offset:8192
	ds_read_b128 v[14:17], v19
	ds_read_b128 v[66:69], v19 offset:8192
	v_bitop3_b32 v19, v124, v120, 4 bitop3:0x36
	v_lshl_or_b32 v19, v19, 4, v18
	v_bitop3_b32 v20, v124, v120, 5 bitop3:0x36
	v_lshl_or_b32 v20, v20, 4, v18
	ds_read_b128 v[70:73], v19
	ds_read_b128 v[78:81], v19 offset:8192
	ds_read_b128 v[74:77], v20
	ds_read_b128 v[82:85], v20 offset:8192
	v_bitop3_b32 v19, v124, v120, 8 bitop3:0x36
	v_lshl_or_b32 v19, v19, 4, v18
	v_bitop3_b32 v20, v124, v120, 9 bitop3:0x36
	v_lshl_or_b32 v20, v20, 4, v18
	ds_read_b128 v[86:89], v19
	ds_read_b128 v[104:107], v19 offset:8192
	ds_read_b128 v[90:93], v20
	ds_read_b128 v[108:111], v20 offset:8192
	v_bitop3_b32 v19, v124, v120, 12 bitop3:0x36
	v_lshl_or_b32 v19, v19, 4, v18
	v_bitop3_b32 v20, v124, v120, 13 bitop3:0x36
	v_lshl_or_b32 v18, v20, 4, v18
	ds_read_b128 v[126:129], v19
	ds_read_b128 v[134:137], v19 offset:8192
	ds_read_b128 v[130:133], v18
	ds_read_b128 v[138:141], v18 offset:8192
	v_mov_b32_e32 v103, 0x7f
	v_lshlrev_b32_e32 v58, 7, v99
	v_or_b32_e32 v122, 0x18000, v117
	s_waitcnt vmcnt(8) lgkmcnt(0)
	v_mfma_scale_f32_32x32x64_f8f6f4 v[18:33], v[2:9], v[10:17], 0, v103, v103 op_sel_hi:[0,0,0]
	v_lshlrev_b32_e32 v125, 3, v119
	v_or_b32_e32 v123, 0x1a000, v117
	v_mfma_scale_f32_32x32x64_f8f6f4 v[2:17], v[2:9], v[62:69], 0, v103, v103 op_sel_hi:[0,0,0]
	v_and_b32_e32 v62, 12, v95
	v_mfma_scale_f32_32x32x64_f8f6f4 v[18:33], v[50:57], v[70:77], v[18:33], v103, v103 op_sel_hi:[0,0,0]
	v_mfma_scale_f32_32x32x64_f8f6f4 v[2:17], v[50:57], v[78:85], v[2:17], v103, v103 op_sel_hi:[0,0,0]
	v_lshl_add_u64 v[50:51], s[10:11], 0, v[58:59]
	v_lshlrev_b32_e32 v58, 4, v119
	v_lshl_add_u64 v[54:55], v[50:51], 0, v[58:59]
	global_load_dwordx4 v[50:53], v[54:55], off
	s_brev_b32 s10, 60
	v_lshlrev_b32_e32 v58, 6, v0
	v_and_b32_e32 v58, 0x4000, v58
	v_or3_b32 v63, v122, v58, v125
	v_or3_b32 v58, v123, v58, v125
	v_mfma_scale_f32_32x32x64_f8f6f4 v[18:33], v[42:49], v[86:93], v[18:33], v103, v103 op_sel_hi:[0,0,0]
	v_mfma_scale_f32_32x32x64_f8f6f4 v[2:17], v[42:49], v[104:111], v[2:17], v103, v103 op_sel_hi:[0,0,0]
	global_load_dwordx4 v[42:45], v[54:55], off offset:32
	global_load_dwordx4 v[46:49], v[54:55], off offset:64
	s_nop 0
	global_load_dwordx4 v[54:57], v[54:55], off offset:96
	v_mfma_scale_f32_32x32x64_f8f6f4 v[2:17], v[34:41], v[134:141], v[2:17], v103, v103 op_sel_hi:[0,0,0]
	v_mfma_scale_f32_32x32x64_f8f6f4 v[18:33], v[34:41], v[126:133], v[18:33], v103, v103 op_sel_hi:[0,0,0]
	s_waitcnt vmcnt(0)
	s_nop 15
	s_nop 1
	v_fma_f32 v2, v2, s10, v50
	v_fma_f32 v3, v3, s10, v51
	v_fma_f32 v4, v4, s10, v52
	v_fma_f32 v5, v5, s10, v53
	v_cvt_pk_f16_f32 v2, v2, v3
	v_cvt_pk_f16_f32 v3, v4, v5
	v_bitop3_b32 v4, v95, v120, 12 bitop3:0x6c
	v_pk_fma_f32 v[18:19], v[18:19], s[10:11], v[50:51] op_sel_hi:[1,0,1]
	v_pk_fma_f32 v[20:21], v[20:21], s[10:11], v[52:53] op_sel_hi:[1,0,1]
	v_lshlrev_b32_e32 v4, 4, v4
	v_cvt_pk_f16_f32 v18, v18, v19
	v_cvt_pk_f16_f32 v19, v20, v21
	v_or_b32_e32 v5, v63, v4
	v_or_b32_e32 v4, v58, v4
	ds_write_b64 v5, v[18:19]
	ds_write_b64 v4, v[2:3]
	v_pk_fma_f32 v[2:3], v[22:23], s[10:11], v[42:43] op_sel_hi:[1,0,1]
	v_pk_fma_f32 v[4:5], v[6:7], s[10:11], v[42:43] op_sel_hi:[1,0,1]
	v_pk_fma_f32 v[6:7], v[24:25], s[10:11], v[44:45] op_sel_hi:[1,0,1]
	v_cvt_pk_f16_f32 v2, v2, v3
	v_cvt_pk_f16_f32 v3, v6, v7
	v_pk_fma_f32 v[6:7], v[8:9], s[10:11], v[44:45] op_sel_hi:[1,0,1]
	v_cvt_pk_f16_f32 v4, v4, v5
	v_cvt_pk_f16_f32 v5, v6, v7
	v_bitop3_b32 v6, v62, v120, 1 bitop3:0x36
	v_lshlrev_b32_e32 v6, 4, v6
	v_or_b32_e32 v7, v63, v6
	ds_write_b64 v7, v[2:3]
	v_or_b32_e32 v2, v58, v6
	ds_write_b64 v2, v[4:5]
	v_pk_fma_f32 v[2:3], v[26:27], s[10:11], v[46:47] op_sel_hi:[1,0,1]
	v_pk_fma_f32 v[6:7], v[28:29], s[10:11], v[48:49] op_sel_hi:[1,0,1]
	v_cvt_pk_f16_f32 v2, v2, v3
	v_pk_fma_f32 v[4:5], v[10:11], s[10:11], v[46:47] op_sel_hi:[1,0,1]
	v_cvt_pk_f16_f32 v3, v6, v7
	v_pk_fma_f32 v[6:7], v[12:13], s[10:11], v[48:49] op_sel_hi:[1,0,1]
	v_cvt_pk_f16_f32 v4, v4, v5
	v_cvt_pk_f16_f32 v5, v6, v7
	v_bitop3_b32 v6, v62, v120, 2 bitop3:0x36
	v_lshlrev_b32_e32 v6, 4, v6
	v_or_b32_e32 v7, v63, v6
	ds_write_b64 v7, v[2:3]
	v_or_b32_e32 v2, v58, v6
	ds_write_b64 v2, v[4:5]
	v_pk_fma_f32 v[2:3], v[30:31], s[10:11], v[54:55] op_sel_hi:[1,0,1]
	v_pk_fma_f32 v[6:7], v[32:33], s[10:11], v[56:57] op_sel_hi:[1,0,1]
	v_cvt_pk_f16_f32 v2, v2, v3
	v_pk_fma_f32 v[4:5], v[14:15], s[10:11], v[54:55] op_sel_hi:[1,0,1]
	v_cvt_pk_f16_f32 v3, v6, v7
	v_pk_fma_f32 v[6:7], v[16:17], s[10:11], v[56:57] op_sel_hi:[1,0,1]
	v_cvt_pk_f16_f32 v4, v4, v5
	v_cvt_pk_f16_f32 v5, v6, v7
	v_bitop3_b32 v6, v62, v120, 3 bitop3:0x36
	v_lshlrev_b32_e32 v6, 4, v6
	v_or_b32_e32 v7, v63, v6
	ds_write_b64 v7, v[2:3]
	v_or_b32_e32 v2, v58, v6
	ds_write_b64 v2, v[4:5]
	v_lshlrev_b32_e32 v2, 8, v101
	s_waitcnt lgkmcnt(0)
	s_barrier
	v_lshrrev_b32_e32 v27, 8, v0
	v_lshrrev_b32_e32 v3, 3, v0
	v_and_b32_e32 v3, 16, v3
	v_mul_u32_u24_e32 v28, 0x60, v27
	v_lshlrev_b32_e32 v26, 5, v27
	v_or_b32_e32 v146, v3, v100
	v_or_b32_e32 v147, v28, v100
	v_or_b32_e32 v4, v146, v26
	v_lshlrev_b32_e32 v209, 2, v4
	v_add_u32_e32 v209, 0x27800, v209
	v_or_b32_e32 v3, v147, v3
	v_lshlrev_b32_e32 v4, 8, v4
	v_add_u32_e32 v3, v3, v60
	v_or_b32_e32 v5, 0x18000, v4
	v_bitop3_b32 v11, v101, v120, 12 bitop3:0x36
	v_or_b32_e32 v95, 0x1c000, v4
	v_lshlrev_b32_e32 v29, 3, v101
	v_lshlrev_b32_e32 v4, 8, v3
	v_lshlrev_b32_e32 v12, 2, v3
	v_bfe_u32 v3, v3, 2, 2
	v_bitop3_b32 v6, v101, v94, v61 bitop3:0x1e
	v_bitop3_b32 v8, v101, v120, 4 bitop3:0x36
	v_bitop3_b32 v10, v101, v120, 8 bitop3:0x36
	v_lshlrev_b32_e32 v94, 4, v11
	v_and_b32_e32 v11, 8, v29
	v_and_or_b32 v3, v12, 12, v3
	v_lshlrev_b32_e32 v6, 4, v6
	v_lshlrev_b32_e32 v8, 4, v8
	v_lshlrev_b32_e32 v58, 4, v10
	v_mad_u32_u24 v4, v119, s17, v4
	v_bitop3_b32 v12, v11, v3, 1 bitop3:0x36
	v_bitop3_b32 v13, v11, v3, 2 bitop3:0x36
	v_bitop3_b32 v14, v11, v3, 3 bitop3:0x36
	v_bitop3_b32 v15, v11, v3, 4 bitop3:0x36
	v_bitop3_b32 v16, v11, v3, 5 bitop3:0x36
	v_bitop3_b32 v17, v11, v3, 6 bitop3:0x36
	v_or_b32_e32 v7, v5, v6
	v_or_b32_e32 v9, v5, v8
	v_or_b32_e32 v10, v5, v58
	v_or_b32_e32 v5, v5, v94
	v_or_b32_e32 v6, v95, v6
	v_or_b32_e32 v60, v95, v8
	v_bitop3_b32 v8, v29, v3, 8 bitop3:0x6c
	v_bitop3_b32 v2, v11, v3, 7 bitop3:0x36
	v_lshl_or_b32 v112, v12, 4, v4
	v_lshl_or_b32 v126, v13, 4, v4
	v_lshl_or_b32 v130, v14, 4, v4
	v_lshl_or_b32 v134, v15, 4, v4
	v_lshl_or_b32 v138, v16, 4, v4
	v_lshl_or_b32 v142, v17, 4, v4
	v_lshl_or_b32 v103, v8, 4, v4
	v_lshl_or_b32 v148, v2, 4, v4
	ds_read_b128 v[22:25], v7
	ds_read_b128 v[18:21], v9
	ds_read_b128 v[14:17], v10
	ds_read_b128 v[10:13], v5
	ds_read_b128 v[6:9], v6
	ds_read_b128 v[2:5], v60
	v_bfe_u32 v103, v0, 6, 1
	s_movk_i32 s5, 0x2000
	v_mbcnt_lo_u32_b32 v30, -1, 0
	v_mbcnt_hi_u32_b32 v32, -1, v30
	v_and_b32_e32 v33, 64, v32
	v_xor_b32_e32 v30, 16, v32
	v_add_u32_e32 v33, 64, v33
	v_cmp_lt_i32_e32 vcc, v30, v33
	v_mad_u32_u24 v44, v103, 48, v147
	v_lshlrev_b32_e32 v60, 8, v44
	v_cndmask_b32_e32 v30, v32, v30, vcc
	v_lshlrev_b32_e32 v30, 2, v30
	v_lshlrev_b32_e32 v44, 2, v44
	v_or_b32_e32 v35, v95, v58
	v_lshlrev_b32_e32 v58, 14, v99
	v_and_b32_e32 v44, 12, v44
	v_xor_b32_e32 v31, 32, v32
	v_cmp_lt_i32_e32 vcc, v31, v33
	v_or_b32_e32 v56, v44, v61
	v_bitop3_b32 v44, v101, v44, v61 bitop3:0x1e
	v_cndmask_b32_e32 v31, v32, v31, vcc
	v_lshl_add_u64 v[32:33], s[8:9], 0, v[58:59]
	v_lshlrev_b32_e32 v58, 4, v98
	v_or_b32_e32 v36, v95, v94
	v_lshl_add_u64 v[88:89], v[32:33], 0, v[58:59]
	v_lshl_or_b32 v57, v44, 4, v60
	ds_read_b128 v[40:43], v35
	ds_read_b128 v[106:109], v36
	s_load_dword s4, s[6:7], 0x0
	global_load_dwordx4 v[36:39], v[88:89], off
	global_load_dwordx4 v[32:35], v[88:89], off offset:1024
	ds_read_b128 v[44:47], v57
	v_bitop3_b32 v48, v101, v56, 4 bitop3:0x36
	v_lshl_or_b32 v62, v48, 4, v60
	ds_read_b128 v[48:51], v62
	v_bitop3_b32 v52, v101, v56, 8 bitop3:0x36
	v_lshl_or_b32 v63, v52, 4, v60
	ds_read_b128 v[52:55], v63
	s_waitcnt lgkmcnt(0)
	v_mfma_f32_16x16x32_f16 v[44:47], v[44:47], v[22:25], 0
	v_bitop3_b32 v64, v101, v56, 12 bitop3:0x36
	ds_read_b128 v[56:59], v57 offset:49152
	v_lshl_or_b32 v60, v64, 4, v60
	v_mfma_f32_16x16x32_f16 v[44:47], v[48:51], v[18:21], v[44:47]
	ds_read_b128 v[68:71], v60
	ds_read_b128 v[72:75], v62 offset:49152
	v_mad_u32_u24 v104, v103, 3, 1
	v_lshlrev_b32_e32 v132, 4, v104
	v_mfma_f32_16x16x32_f16 v[44:47], v[52:55], v[14:17], v[44:47]
	v_add_u32_e32 v52, v132, v147
	global_load_dwordx4 v[64:67], v[88:89], off offset:2048
	global_load_dwordx4 v[48:51], v[88:89], off offset:3072
	ds_read_b128 v[76:79], v63 offset:49152
	ds_read_b128 v[80:83], v60 offset:49152
	s_waitcnt lgkmcnt(3)
	v_mfma_f32_16x16x32_f16 v[44:47], v[68:71], v[10:13], v[44:47]
	v_lshlrev_b32_e32 v60, 8, v52
	v_lshlrev_b32_e32 v52, 2, v52
	v_and_b32_e32 v52, 12, v52
	v_mfma_f32_16x16x32_f16 v[44:47], v[56:59], v[6:9], v[44:47]
	v_or_b32_e32 v62, v52, v61
	v_bitop3_b32 v52, v101, v52, v61 bitop3:0x1e
	v_lshl_or_b32 v63, v52, 4, v60
	s_waitcnt lgkmcnt(2)
	v_mfma_f32_16x16x32_f16 v[44:47], v[72:75], v[2:5], v[44:47]
	ds_read_b128 v[52:55], v63
	v_bitop3_b32 v56, v101, v62, 4 bitop3:0x36
	v_lshl_or_b32 v84, v56, 4, v60
	s_waitcnt lgkmcnt(2)
	v_mfma_f32_16x16x32_f16 v[44:47], v[76:79], v[40:43], v[44:47]
	ds_read_b128 v[56:59], v84
	v_bitop3_b32 v68, v101, v62, 8 bitop3:0x36
	v_lshl_or_b32 v85, v68, 4, v60
	s_waitcnt lgkmcnt(2)
	v_mfma_f32_16x16x32_f16 v[110:113], v[80:83], v[106:109], v[44:47]
	ds_read_b128 v[68:71], v63 offset:49152
	v_bitop3_b32 v62, v101, v62, 12 bitop3:0x36
	v_lshl_or_b32 v60, v62, 4, v60
	ds_read_b128 v[44:47], v85
	s_waitcnt lgkmcnt(3)
	v_mfma_f32_16x16x32_f16 v[52:55], v[52:55], v[22:25], 0
	ds_read_b128 v[72:75], v60
	ds_read_b128 v[76:79], v84 offset:49152
	v_mad_u32_u24 v105, v103, 3, 2
	v_lshlrev_b32_e32 v133, 4, v105
	s_waitcnt lgkmcnt(4)
	v_mfma_f32_16x16x32_f16 v[52:55], v[56:59], v[18:21], v[52:55]
	ds_read_b128 v[56:59], v85 offset:49152
	v_add_co_u32_e32 v114, vcc, s15, v88
	s_waitcnt lgkmcnt(3)
	v_mfma_f32_16x16x32_f16 v[44:47], v[44:47], v[14:17], v[52:55]
	v_addc_co_u32_e32 v115, vcc, 0, v89, vcc
	v_lshlrev_b32_e32 v31, 2, v31
	s_waitcnt lgkmcnt(2)
	v_mfma_f32_16x16x32_f16 v[44:47], v[72:75], v[10:13], v[44:47]
	ds_read_b128 v[52:55], v60 offset:49152
	v_add_u32_e32 v60, v133, v147
	v_lshlrev_b32_e32 v72, 8, v60
	v_lshlrev_b32_e32 v60, 2, v60
	v_mfma_f32_16x16x32_f16 v[44:47], v[68:71], v[6:9], v[44:47]
	v_and_b32_e32 v60, 12, v60
	v_or_b32_e32 v68, v60, v61
	v_bitop3_b32 v60, v101, v60, v61 bitop3:0x1e
	v_lshl_or_b32 v69, v60, 4, v72
	s_waitcnt lgkmcnt(2)
	v_mfma_f32_16x16x32_f16 v[44:47], v[76:79], v[2:5], v[44:47]
	ds_read_b128 v[60:63], v69
	v_bitop3_b32 v70, v101, v68, 4 bitop3:0x36
	v_lshl_or_b32 v70, v70, 4, v72
	s_waitcnt lgkmcnt(2)
	v_mfma_f32_16x16x32_f16 v[44:47], v[56:59], v[40:43], v[44:47]
	ds_read_b128 v[56:59], v70
	v_bitop3_b32 v71, v101, v68, 8 bitop3:0x36
	v_lshl_or_b32 v71, v71, 4, v72
	s_waitcnt lgkmcnt(1)
	v_mfma_f32_16x16x32_f16 v[22:25], v[60:63], v[22:25], 0
	v_bitop3_b32 v60, v101, v68, 12 bitop3:0x36
	v_lshl_or_b32 v68, v60, 4, v72
	ds_read_b32 v210, v209
	v_mfma_f32_16x16x32_f16 v[126:129], v[52:55], v[106:109], v[44:47]
	s_nop 2
	ds_read_b128 v[44:47], v71
	ds_read_b128 v[52:55], v69 offset:49152
	ds_read_b128 v[60:63], v70 offset:49152
	s_waitcnt lgkmcnt(4)
	v_mfma_f32_16x16x32_f16 v[18:21], v[56:59], v[18:21], v[22:25]
	ds_read_b128 v[56:59], v71 offset:49152
	s_nop 1
	ds_read_b128 v[22:25], v68
	s_waitcnt lgkmcnt(4)
	v_mfma_f32_16x16x32_f16 v[14:17], v[44:47], v[14:17], v[18:21]
	v_add_co_u32_e32 v44, vcc, s5, v88
	s_movk_i32 s5, 0x3000
	s_nop 0
	ds_read_b128 v[18:21], v68 offset:49152
	s_waitcnt lgkmcnt(1)
	v_mfma_f32_16x16x32_f16 v[10:13], v[22:25], v[10:13], v[14:17]
	v_addc_co_u32_e32 v45, vcc, 0, v89, vcc
	global_load_dwordx4 v[84:87], v[114:115], off offset:1024
	global_load_dwordx4 v[80:83], v[114:115], off offset:2048
	global_load_dwordx4 v[92:95], v[44:45], off offset:-4096
	global_load_dwordx4 v[76:79], v[44:45], off
	v_mfma_f32_16x16x32_f16 v[6:9], v[52:55], v[6:9], v[10:13]
	global_load_dwordx4 v[72:75], v[44:45], off offset:1024
	global_load_dwordx4 v[68:71], v[44:45], off offset:2048
	global_load_dwordx4 v[52:55], v[44:45], off offset:3072
	v_mov_b32_e32 v13, 0xff61b1e6
	v_mfma_f32_16x16x32_f16 v[2:5], v[60:63], v[2:5], v[6:9]
	s_nop 2
	v_add_co_u32_e32 v6, vcc, s5, v88
	v_mfma_f32_16x16x32_f16 v[2:5], v[56:59], v[40:43], v[2:5]
	s_nop 0
	v_addc_co_u32_e32 v7, vcc, 0, v89, vcc
	global_load_dwordx4 v[88:91], v[114:115], off offset:3072
	global_load_dwordx4 v[60:63], v[6:7], off
	global_load_dwordx4 v[56:59], v[6:7], off offset:1024
	global_load_dwordx4 v[44:47], v[6:7], off offset:2048
	global_load_dwordx4 v[40:43], v[6:7], off offset:3072
	s_waitcnt lgkmcnt(0)
	v_mfma_f32_16x16x32_f16 v[16:19], v[18:21], v[106:109], v[2:5]
	s_mov_b32 s5, 0xff61b1e6
	s_nop 0
	v_or_b32_e32 v3, s14, v146
	v_mov_b32_e32 v4, 0x7df
	v_med3_u32 v3, v3, 32, v4
	v_or_b32_e32 v4, v97, v102
	v_sub_u32_e32 v3, v4, v3
	v_add_f32_e32 v2, s4, v210
	v_add_u32_e32 v3, 32, v3
	v_mad_u32_u24 v4, v103, 48, v3
	s_movk_i32 s4, 0x41
	v_add_f32_e32 v5, v2, v110
	v_mul_f32_e32 v5, 0x3db8aa3b, v5
	v_cmp_gt_u32_e32 vcc, s4, v4
	v_add_u32_e32 v6, 1, v4
	v_add_f32_e32 v7, v2, v111
	v_cndmask_b32_e32 v5, v13, v5, vcc
	v_mul_f32_e32 v7, 0x3db8aa3b, v7
	v_cmp_gt_u32_e32 vcc, s4, v6
	v_add_u32_e32 v8, 2, v4
	v_add_f32_e32 v9, v2, v112
	v_cndmask_b32_e32 v6, v13, v7, vcc
	v_mul_f32_e32 v9, 0x3db8aa3b, v9
	v_cmp_gt_u32_e32 vcc, s4, v8
	v_add_u32_e32 v4, 3, v4
	v_max3_f32 v7, v5, s5, v6
	v_cndmask_b32_e32 v8, v13, v9, vcc
	v_add_f32_e32 v9, v2, v113
	v_mul_f32_e32 v9, 0x3db8aa3b, v9
	v_cmp_gt_u32_e32 vcc, s4, v4
	v_add_u32_e32 v11, v3, v132
	v_add_f32_e32 v12, v2, v127
	v_cndmask_b32_e32 v10, v13, v9, vcc
	v_max3_f32 v4, v7, v8, v10
	v_add_f32_e32 v7, v2, v126
	v_mul_f32_e32 v7, 0x3db8aa3b, v7
	v_cmp_gt_u32_e32 vcc, s4, v11
	v_add_u32_e32 v9, 1, v11
	v_mul_f32_e32 v12, 0x3db8aa3b, v12
	v_cndmask_b32_e32 v7, v13, v7, vcc
	v_cmp_gt_u32_e32 vcc, s4, v9
	v_add_f32_e32 v14, v2, v128
	v_mul_f32_e32 v14, 0x3db8aa3b, v14
	v_cndmask_b32_e32 v9, v13, v12, vcc
	v_add_u32_e32 v12, 2, v11
	v_cmp_gt_u32_e32 vcc, s4, v12
	v_add_u32_e32 v11, 3, v11
	v_add_u32_e32 v3, v3, v133
	v_cndmask_b32_e32 v12, v13, v14, vcc
	v_add_f32_e32 v14, v2, v129
	v_mul_f32_e32 v14, 0x3db8aa3b, v14
	v_cmp_gt_u32_e32 vcc, s4, v11
	v_add_f32_e32 v11, v2, v16
	v_mul_f32_e32 v11, 0x3db8aa3b, v11
	v_cndmask_b32_e32 v15, v13, v14, vcc
	v_cmp_gt_u32_e32 vcc, s4, v3
	v_add_u32_e32 v14, 1, v3
	v_add_f32_e32 v16, v2, v17
	v_cndmask_b32_e32 v11, v13, v11, vcc
	v_mul_f32_e32 v16, 0x3db8aa3b, v16
	v_cmp_gt_u32_e32 vcc, s4, v14
	v_add_f32_e32 v17, v2, v18
	v_max3_f32 v4, v4, v7, v9
	v_cndmask_b32_e32 v14, v13, v16, vcc
	v_add_u32_e32 v16, 2, v3
	v_mul_f32_e32 v17, 0x3db8aa3b, v17
	v_cmp_gt_u32_e32 vcc, s4, v16
	v_add_u32_e32 v3, 3, v3
	v_add_f32_e32 v2, v2, v19
	v_max3_f32 v4, v4, v12, v15
	v_cndmask_b32_e32 v16, v13, v17, vcc
	v_mul_f32_e32 v2, 0x3db8aa3b, v2
	v_cmp_gt_u32_e32 vcc, s4, v3
	v_max3_f32 v4, v4, v11, v14
	v_lshlrev_b32_e32 v126, 5, v99
	v_cndmask_b32_e32 v17, v13, v2, vcc
	v_max3_f32 v2, v4, v16, v17
	v_mov_b32_e32 v3, v2
	v_lshlrev_b32_e32 v127, 2, v119
	v_lshrrev_b32_e32 v4, 7, v0
	v_cmp_gt_u32_e32 vcc, 16, v98
	v_permlane16_swap_b32_e32 v3, v2
	v_max_f32_e32 v2, v2, v3
	v_mov_b32_e32 v3, v2
	s_nop 1
	v_permlane32_swap_b32_e32 v3, v2
	v_max_f32_e32 v13, v2, v3
	v_and_b32_e32 v2, 0x180, v0
	v_or_b32_e32 v2, 0x23400, v2
	v_lshlrev_b32_e32 v3, 2, v100
	s_and_saveexec_b64 s[4:5], vcc
	v_lshlrev_b32_e32 v18, 6, v103
	v_add3_u32 v18, v2, v18, v3
	ds_write_b32 v18, v13
	s_or_b64 exec, exec, s[4:5]
	v_lshlrev_b32_e32 v18, 4, v103
	v_bitop3_b32 v19, v18, 16, v100 bitop3:0x36
	v_lshl_add_u32 v2, v19, 2, v2
	s_waitcnt lgkmcnt(0)
	s_barrier
	ds_read_b32 v19, v2
	v_max_f32_e32 v13, v13, v13
	v_mul_u32_u24_e32 v20, 0xd00, v4
	s_load_dwordx2 s[0:1], s[0:1], 0x30
	v_or_b32_e32 v2, 1, v124
	s_waitcnt lgkmcnt(0)
	v_max_f32_e32 v19, v19, v19
	v_max_f32_e32 v19, v13, v19
	v_sub_f32_e32 v5, v5, v19
	v_exp_f32_e32 v5, v5
	v_sub_f32_e32 v6, v6, v19
	v_exp_f32_e32 v6, v6
	v_sub_f32_e32 v8, v8, v19
	v_mul_u32_u24_e32 v13, 0xd0, v100
	v_exp_f32_e32 v8, v8
	v_sub_f32_e32 v10, v10, v19
	v_add3_u32 v20, v13, v20, v29
	v_exp_f32_e32 v10, v10
	v_or_b32_e32 v22, 0x20000, v20
	v_add_f32_e32 v20, 0, v5
	v_add_f32_e32 v20, v20, v6
	v_add_f32_e32 v20, v20, v8
	v_add_f32_e32 v23, v20, v10
	v_cvt_pk_f16_f32 v21, v8, v10
	v_cvt_pk_f16_f32 v20, v5, v6
	v_mad_u32_u24 v5, v103, s16, v22
	ds_write_b64 v5, v[20:21]
	v_sub_f32_e32 v5, v7, v19
	v_exp_f32_e32 v5, v5
	v_sub_f32_e32 v6, v9, v19
	v_exp_f32_e32 v6, v6
	v_sub_f32_e32 v7, v12, v19
	v_exp_f32_e32 v7, v7
	v_sub_f32_e32 v8, v15, v19
	v_exp_f32_e32 v8, v8
	v_sub_f32_e32 v10, v11, v19
	v_add_f32_e32 v9, v23, v5
	v_exp_f32_e32 v10, v10
	v_sub_f32_e32 v11, v14, v19
	v_add_f32_e32 v9, v9, v6
	v_exp_f32_e32 v11, v11
	v_sub_f32_e32 v12, v16, v19
	v_add_f32_e32 v9, v9, v7
	v_exp_f32_e32 v12, v12
	v_sub_f32_e32 v14, v17, v19
	v_add_f32_e32 v9, v9, v8
	v_exp_f32_e32 v14, v14
	v_add_f32_e32 v9, v9, v10
	v_add_f32_e32 v9, v9, v11
	v_add_f32_e32 v9, v9, v12
	v_add_f32_e32 v9, v9, v14
	v_mov_b32_e32 v15, v9
	v_cvt_pk_f16_f32 v7, v7, v8
	v_cvt_pk_f16_f32 v6, v5, v6
	v_lshl_add_u32 v5, v104, 5, v22
	ds_write_b64 v5, v[6:7]
	v_permlane16_swap_b32_e32 v15, v9
	v_add_f32_e32 v5, v9, v15
	v_mov_b32_e32 v6, v5
	s_movk_i32 s7, 0xd00
	s_mov_b32 s6, 0x20000
	v_cvt_pk_f16_f32 v9, v12, v14
	v_cvt_pk_f16_f32 v8, v10, v11
	v_lshl_add_u32 v7, v105, 5, v22
	ds_write_b64 v7, v[8:9]
	v_permlane32_swap_b32_e32 v6, v5
	s_and_saveexec_b64 s[4:5], vcc
	s_cbranch_execz .LBB1_4
	v_lshlrev_b32_e32 v4, 5, v4
	v_or_b32_e32 v7, v18, v100
	v_lshlrev_b32_e32 v4, 2, v4
	v_lshlrev_b32_e32 v7, 2, v7
	s_mov_b32 s8, 0x23600
	v_add3_u32 v4, v7, v4, s8
	v_add_f32_e32 v5, v5, v6
	ds_write_b32 v4, v5
